# speedup vs baseline: 1.1357x; 1.0096x over previous
_Z10qkv_kernelPKfS0_S0_PKdPKtS0_PhPfS6_:
	s_load_dwordx2 s[8:9], s[0:1], 0x0
	s_load_dwordx4 s[4:7], s[0:1], 0x18
	s_load_dwordx4 s[20:23], s[0:1], 0x8
	v_lshrrev_b32_e32 v1, 6, v0
	v_and_b32_e32 v146, 63, v0
	v_lshlrev_b32_e32 v134, 14, v1
	v_mov_b32_e32 v135, 0
	s_waitcnt lgkmcnt(0)
	v_lshrrev_b32_e32 v188, 6, v0
	v_and_b32_e32 v189, 31, v0
	v_lshl_add_u32 v188, v188, 5, v189
	v_lshlrev_b32_e32 v188, 2, v188
	global_load_dword v190, v188, s[20:21]
	global_load_dword v191, v188, s[22:23]
	v_lshl_add_u64 v[2:3], s[6:7], 0, v[134:135]
	v_lshlrev_b32_e32 v134, 4, v146
	s_ashr_i32 s6, s2, 6
	v_lshl_add_u64 v[132:133], v[2:3], 0, v[134:135]
	v_lshl_or_b32 v2, s6, 3, v1
	v_ashrrev_i32_e32 v3, 31, v2
	v_lshlrev_b64 v[2:3], 10, v[2:3]
	v_lshl_add_u64 v[2:3], s[4:5], 0, v[2:3]
	v_lshl_add_u64 v[2:3], v[2:3], 0, v[134:135]
	global_load_dwordx4 v[94:97], v[132:133], off
	global_load_dwordx4 v[86:89], v[132:133], off offset:1024
	global_load_dwordx4 v[54:57], v[132:133], off offset:2048
	global_load_dwordx4 v[42:45], v[132:133], off offset:3072
	global_load_dwordx4 v[98:101], v[2:3], off
	s_movk_i32 s7, 0x1000
	v_add_co_u32_e32 v2, vcc, s7, v132
	s_lshl_b32 s3, s2, 6
	s_nop 0
	v_addc_co_u32_e32 v3, vcc, 0, v133, vcc
	s_movk_i32 s4, 0x2000
	v_add_co_u32_e32 v4, vcc, s4, v132
	s_and_b32 s3, s3, 0xfc0
	s_nop 0
	v_addc_co_u32_e32 v5, vcc, 0, v133, vcc
	s_movk_i32 s4, 0x3000
	s_ashr_i32 s7, s6, 31
	s_lshl_b32 s16, s3, 2
	v_add_co_u32_e32 v4, vcc, s4, v132
	v_and_b32_e32 v106, 7, v0
	s_add_u32 s4, s8, s16
	v_addc_co_u32_e32 v5, vcc, 0, v133, vcc
	s_addc_u32 s5, s9, 0
	v_lshlrev_b32_e32 v2, 5, v106
	v_mov_b32_e32 v3, v135
	v_lshrrev_b32_e32 v107, 3, v0
	v_lshl_add_u64 v[2:3], s[4:5], 0, v[2:3]
	s_lshl_b64 s[4:5], s[6:7], 22
	v_lshl_or_b32 v4, v107, 14, s4
	v_mov_b32_e32 v5, s5
	v_lshl_add_u64 v[2:3], v[2:3], 0, v[4:5]
	s_mov_b64 s[4:5], 0x100000
	v_lshl_add_u64 v[4:5], v[2:3], 0, s[4:5]
	s_mov_b32 s4, 0x100000
	v_add_co_u32_e32 v6, vcc, s4, v2
	s_mov_b64 s[4:5], 0x200000
	s_nop 0
	v_addc_co_u32_e32 v7, vcc, 0, v3, vcc
	global_load_dwordx4 v[26:29], v[2:3], off offset:16
	global_load_dwordx4 v[30:33], v[2:3], off
	global_load_dwordx4 v[22:25], v[6:7], off
	global_load_dwordx4 v[18:21], v[4:5], off offset:16
	v_lshl_add_u64 v[4:5], v[2:3], 0, s[4:5]
	s_mov_b32 s4, 0x200000
	v_add_co_u32_e32 v6, vcc, s4, v2
	s_mov_b64 s[4:5], 0x300000
	s_nop 0
	v_addc_co_u32_e32 v7, vcc, 0, v3, vcc
	v_lshl_add_u64 v[102:103], v[2:3], 0, s[4:5]
	s_mov_b32 s4, 0x300000
	v_add_co_u32_e32 v104, vcc, s4, v2
	global_load_dwordx4 v[14:17], v[6:7], off
	global_load_dwordx4 v[10:13], v[4:5], off offset:16
	v_addc_co_u32_e32 v105, vcc, 0, v3, vcc
	global_load_dwordx4 v[6:9], v[104:105], off
	global_load_dwordx4 v[2:5], v[102:103], off offset:16
	s_mov_b64 s[24:25], 0x1000
	s_mov_b64 s[26:27], 0x2000
	s_mov_b64 s[28:29], 0x3000
	v_lshl_add_u64 v[182:183], v[132:133], 0, s[24:25]
	v_lshl_add_u64 v[184:185], v[132:133], 0, s[26:27]
	v_lshl_add_u64 v[186:187], v[132:133], 0, s[28:29]
	global_load_dwordx4 v[78:81], v[182:183], off offset:1024
	global_load_dwordx4 v[82:85], v[182:183], off offset:2048
	global_load_dwordx4 v[74:77], v[182:183], off offset:3072
	global_load_dwordx4 v[90:93], v[184:185], off offset:-4096
	global_load_dwordx4 v[66:69], v[184:185], off
	global_load_dwordx4 v[70:73], v[184:185], off offset:1024
	global_load_dwordx4 v[62:65], v[184:185], off offset:2048
	global_load_dwordx4 v[58:61], v[184:185], off offset:3072
	global_load_dwordx4 v[50:53], v[186:187], off
	global_load_dwordx4 v[46:49], v[186:187], off offset:1024
	global_load_dwordx4 v[38:41], v[186:187], off offset:2048
	global_load_dwordx4 v[34:37], v[186:187], off offset:3072
	v_mbcnt_lo_u32_b32 v102, -1, 0
	v_mbcnt_hi_u32_b32 v108, -1, v102
	v_and_b32_e32 v102, 64, v108
	v_add_u32_e32 v109, 64, v102
	v_xor_b32_e32 v102, 32, v108
	v_cmp_lt_i32_e32 vcc, v102, v109
	s_load_dwordx2 s[8:9], s[0:1], 0x28
	v_cmp_lt_u32_e64 s[4:5], 31, v146
	v_cndmask_b32_e32 v102, v108, v102, vcc
	v_lshlrev_b32_e32 v105, 2, v102
	v_lshlrev_b32_e32 v130, 5, v1
	s_waitcnt vmcnt(20)
	ds_bpermute_b32 v102, v105, v98
	ds_bpermute_b32 v103, v105, v99
	ds_bpermute_b32 v104, v105, v100
	ds_bpermute_b32 v105, v105, v101
	s_waitcnt lgkmcnt(0)
	v_add_f64 v[98:99], v[98:99], v[102:103]
	v_xor_b32_e32 v102, 16, v108
	v_cmp_lt_i32_e32 vcc, v102, v109
	v_add_f64 v[100:101], v[100:101], v[104:105]
	s_nop 0
	v_cndmask_b32_e32 v102, v108, v102, vcc
	v_lshlrev_b32_e32 v141, 2, v102
	ds_bpermute_b32 v102, v141, v98
	ds_bpermute_b32 v103, v141, v99
	ds_bpermute_b32 v104, v141, v100
	ds_bpermute_b32 v105, v141, v101
	s_waitcnt lgkmcnt(2)
	v_add_f64 v[98:99], v[98:99], v[102:103]
	v_xor_b32_e32 v102, 8, v108
	v_cmp_lt_i32_e32 vcc, v102, v109
	s_waitcnt lgkmcnt(0)
	v_add_f64 v[100:101], v[100:101], v[104:105]
	v_cndmask_b32_e32 v102, v108, v102, vcc
	v_lshlrev_b32_e32 v142, 2, v102
	ds_bpermute_b32 v102, v142, v98
	ds_bpermute_b32 v103, v142, v99
	ds_bpermute_b32 v104, v142, v100
	ds_bpermute_b32 v105, v142, v101
	s_waitcnt lgkmcnt(2)
	v_add_f64 v[98:99], v[98:99], v[102:103]
	v_xor_b32_e32 v102, 4, v108
	v_cmp_lt_i32_e32 vcc, v102, v109
	s_waitcnt lgkmcnt(0)
	v_add_f64 v[100:101], v[100:101], v[104:105]
	v_cndmask_b32_e32 v102, v108, v102, vcc
	v_lshlrev_b32_e32 v143, 2, v102
	ds_bpermute_b32 v102, v143, v98
	ds_bpermute_b32 v103, v143, v99
	ds_bpermute_b32 v104, v143, v100
	ds_bpermute_b32 v105, v143, v101
	s_waitcnt lgkmcnt(2)
	v_add_f64 v[98:99], v[98:99], v[102:103]
	v_xor_b32_e32 v102, 2, v108
	v_cmp_lt_i32_e32 vcc, v102, v109
	s_waitcnt lgkmcnt(0)
	v_add_f64 v[100:101], v[100:101], v[104:105]
	v_cndmask_b32_e32 v102, v108, v102, vcc
	v_lshlrev_b32_e32 v144, 2, v102
	ds_bpermute_b32 v102, v144, v98
	ds_bpermute_b32 v103, v144, v99
	ds_bpermute_b32 v104, v144, v100
	ds_bpermute_b32 v105, v144, v101
	s_waitcnt lgkmcnt(2)
	v_add_f64 v[98:99], v[98:99], v[102:103]
	v_xor_b32_e32 v102, 1, v108
	v_cmp_lt_i32_e32 vcc, v102, v109
	s_waitcnt lgkmcnt(0)
	v_add_f64 v[100:101], v[100:101], v[104:105]
	v_cndmask_b32_e32 v102, v108, v102, vcc
	v_lshlrev_b32_e32 v145, 2, v102
	ds_bpermute_b32 v102, v145, v98
	ds_bpermute_b32 v103, v145, v99
	ds_bpermute_b32 v104, v145, v100
	ds_bpermute_b32 v105, v145, v101
	v_cmp_gt_u32_e32 vcc, 32, v146
	s_and_saveexec_b64 s[10:11], s[4:5]
	s_xor_b64 s[4:5], exec, s[10:11]
	v_lshlrev_b32_e32 v130, 5, v1
	s_or_saveexec_b64 s[10:11], s[4:5]
	s_load_dwordx2 s[14:15], s[0:1], 0x38
	s_xor_b64 exec, exec, s[10:11]
	s_cbranch_execz .LBB1_4
	s_load_dwordx4 s[20:23], s[0:1], 0x8
	v_or_b32_e32 v108, v130, v146
	v_lshlrev_b32_e32 v108, 2, v108
	s_waitcnt lgkmcnt(0)
	v_add_f64 v[98:99], v[98:99], v[102:103]
	s_movk_i32 s12, 0xffef
	s_mov_b32 s4, 0
	v_ldexp_f64 v[98:99], v[98:99], s12
	v_add_f64 v[100:101], v[100:101], v[104:105]
	s_mov_b32 s5, 0x3ee00000
	v_mul_f64 v[102:103], v[98:99], v[98:99]
	v_fma_f64 v[100:101], v[100:101], s[4:5], -v[102:103]
	v_cvt_f32_f64_e32 v100, v[100:101]
	s_mov_b32 s13, 0x800000
	v_add_f32_e32 v100, 0x3727c5ac, v100
	v_mul_f32_e32 v101, 0x4b800000, v100
	v_cmp_gt_f32_e64 s[4:5], s13, v100
	v_cvt_f32_f64_e32 v98, v[98:99]
	s_nop 0
	v_cndmask_b32_e64 v100, v100, v101, s[4:5]
	v_rsq_f32_e32 v100, v100
	v_add_u32_e32 v101, 0, v108
	v_mul_f32_e32 v102, 0x45800000, v100
	v_cndmask_b32_e64 v100, v100, v102, s[4:5]
	v_mul_f32_e32 v100, v100, v190
	v_fma_f32 v98, -v100, v98, v191
	ds_write2st64_b32 v101, v100, v98 offset0:128 offset1:132
.LBB1_4:
	s_or_b64 exec, exec, s[10:11]
	s_waitcnt lgkmcnt(0)
	v_lshrrev_b32_e32 v103, 4, v0
	v_bfe_u32 v104, v0, 3, 2
	v_lshlrev_b32_e32 v102, 4, v0
	v_and_or_b32 v103, v103, 4, v104
	v_lshl_add_u32 v105, v107, 2, 0
	v_lshlrev_b32_e32 v103, 6, v103
	v_and_b32_e32 v102, 48, v102
	s_barrier
	ds_read2st64_b32 v[98:99], v105 offset0:128 offset1:129
	ds_read2st64_b32 v[100:101], v105 offset0:132 offset1:133
	v_add3_u32 v109, 0, v103, v102
	ds_read2st64_b32 v[102:103], v105 offset0:134 offset1:135
	ds_read2st64_b32 v[104:105], v105 offset0:130 offset1:131
	s_movk_i32 s4, 0x70
	v_lshrrev_b32_e32 v108, 5, v146
	s_waitcnt vmcnt(17) lgkmcnt(2)
	v_fma_f32 v22, v22, v99, v101
	v_fma_f32 v23, v23, v99, v101
	s_waitcnt vmcnt(15) lgkmcnt(0)
	v_fma_f32 v14, v14, v104, v102
	v_fma_f32 v15, v15, v104, v102
	v_cvt_pk_bf16_f32 v22, v22, v23
	v_fma_f32 v23, v24, v99, v101
	v_fma_f32 v24, v25, v99, v101
	v_fma_f32 v18, v18, v99, v101
	v_fma_f32 v19, v19, v99, v101
	v_cvt_pk_bf16_f32 v14, v14, v15
	v_fma_f32 v15, v16, v104, v102
	v_fma_f32 v16, v17, v104, v102
	s_waitcnt vmcnt(14)
	v_fma_f32 v10, v10, v104, v102
	v_fma_f32 v11, v11, v104, v102
	s_waitcnt vmcnt(13)
	v_fma_f32 v6, v6, v105, v103
	v_fma_f32 v7, v7, v105, v103
	v_fma_f32 v30, v30, v98, v100
	v_fma_f32 v31, v31, v98, v100
	v_fma_f32 v32, v32, v98, v100
	v_fma_f32 v33, v33, v98, v100
	v_fma_f32 v26, v26, v98, v100
	v_fma_f32 v27, v27, v98, v100
	v_cvt_pk_bf16_f32 v23, v23, v24
	v_cvt_pk_bf16_f32 v24, v18, v19
	v_fma_f32 v18, v20, v99, v101
	v_fmac_f32_e32 v101, v21, v99
	v_cvt_pk_bf16_f32 v15, v15, v16
	v_cvt_pk_bf16_f32 v16, v10, v11
	v_fma_f32 v10, v12, v104, v102
	v_fma_f32 v11, v13, v104, v102
	v_cvt_pk_bf16_f32 v6, v6, v7
	v_fma_f32 v7, v8, v105, v103
	v_fma_f32 v8, v9, v105, v103
	s_waitcnt vmcnt(12)
	v_fma_f32 v2, v2, v105, v103
	v_fma_f32 v3, v3, v105, v103
	v_cvt_pk_bf16_f32 v30, v30, v31
	v_cvt_pk_bf16_f32 v31, v32, v33
	v_cvt_pk_bf16_f32 v32, v26, v27
	v_fma_f32 v26, v28, v98, v100
	v_fma_f32 v27, v29, v98, v100
	v_cvt_pk_bf16_f32 v25, v18, v101
	v_bitop3_b32 v18, v107, s4, 64 bitop3:0xc8
	v_cvt_pk_bf16_f32 v17, v10, v11
	s_movk_i32 s4, 0xb0
	v_mov_b32_e32 v10, 0x80
	v_cvt_pk_bf16_f32 v7, v7, v8
	v_cvt_pk_bf16_f32 v8, v2, v3
	v_fma_f32 v2, v4, v105, v103
	v_fmac_f32_e32 v103, v5, v105
	v_cvt_pk_bf16_f32 v33, v26, v27
	v_lshlrev_b32_e32 v27, 1, v107
	v_bitop3_b32 v10, v107, s4, v10 bitop3:0xc8
	v_cvt_pk_bf16_f32 v9, v2, v103
	s_movk_i32 s4, 0xf0
	v_mov_b32_e32 v2, 0xc0
	v_and_b32_e32 v26, 48, v107
	v_and_b32_e32 v27, 8, v27
	v_bitop3_b32 v2, v107, s4, v2 bitop3:0xc8
	v_or3_b32 v26, v26, v27, v106
	v_or3_b32 v18, v18, v27, v106
	v_or3_b32 v10, v10, v27, v106
	v_or3_b32 v2, v2, v27, v106
	v_lshlrev_b32_e32 v26, 7, v26
	v_lshlrev_b32_e32 v18, 7, v18
	v_lshlrev_b32_e32 v10, 7, v10
	v_lshlrev_b32_e32 v2, 7, v2
	v_and_b32_e32 v26, 0x1e00, v26
	v_and_b32_e32 v18, 0x3e00, v18
	v_and_b32_e32 v10, 0x5e00, v10
	v_and_b32_e32 v2, 0x7e00, v2
	v_add_u32_e32 v26, v109, v26
	v_add_u32_e32 v18, v109, v18
	v_add_u32_e32 v10, v109, v10
	v_add_u32_e32 v2, v109, v2
	v_mov_b32_e32 v131, 0
	ds_write_b128 v26, v[30:33]
	ds_write_b128 v18, v[22:25]
	ds_write_b128 v10, v[14:17]
	ds_write_b128 v2, v[6:9]
	v_lshl_add_u64 v[2:3], v[130:131], 2, s[8:9]
	v_lshlrev_b32_e32 v136, 4, v108
	v_mov_b32_e32 v137, v131
	v_lshl_add_u64 v[138:139], v[2:3], 0, v[136:137]
	s_waitcnt lgkmcnt(0)
	s_barrier
	global_load_dwordx4 v[2:5], v[138:139], off
	global_load_dwordx4 v[6:9], v[138:139], off offset:32
	global_load_dwordx4 v[10:13], v[138:139], off offset:64
	global_load_dwordx4 v[14:17], v[138:139], off offset:96
	v_lshlrev_b32_e32 v18, 3, v146
	v_and_b32_e32 v19, 24, v18
	v_and_b32_e32 v20, 0xc0, v134
	v_lshlrev_b32_e32 v21, 1, v0
	v_and_b32_e32 v21, 32, v21
	v_and_b32_e32 v18, 0x100, v18
	v_add3_u32 v19, 0, v19, v20
	v_add3_u32 v140, v19, v21, v18
	ds_read_b64_tr_b16 v[98:99], v140
	ds_read_b64_tr_b16 v[100:101], v140 offset:1024
	ds_read_b64_tr_b16 v[104:105], v140 offset:1536
	ds_read_b64_tr_b16 v[102:103], v140 offset:512
	s_waitcnt vmcnt(0) lgkmcnt(2)
	v_mfma_f32_32x32x16_bf16 v[18:33], v[94:97], v[98:101], v[2:17]
	ds_read_b64_tr_b16 v[98:99], v140 offset:2048
	ds_read_b64_tr_b16 v[100:101], v140 offset:3072
	ds_read_b64_tr_b16 v[108:109], v140 offset:3584
	ds_read_b64_tr_b16 v[106:107], v140 offset:2560
	s_mov_b32 s4, 0x20000
	v_and_b32_e32 v137, 31, v0
	s_waitcnt lgkmcnt(2)
	v_mfma_f32_32x32x16_bf16 v[18:33], v[86:89], v[98:101], v[18:33]
	ds_read_b64_tr_b16 v[98:99], v140 offset:4096
	ds_read_b64_tr_b16 v[100:101], v140 offset:5120
	ds_read_b64_tr_b16 v[112:113], v140 offset:5632
	ds_read_b64_tr_b16 v[110:111], v140 offset:4608
	s_waitcnt lgkmcnt(2)
	v_mfma_f32_32x32x16_bf16 v[18:33], v[54:57], v[98:101], v[18:33]
	v_mfma_f32_32x32x16_bf16 v[2:17], v[94:97], v[102:105], v[2:17]
	ds_read_b64_tr_b16 v[94:95], v140 offset:6144
	ds_read_b64_tr_b16 v[96:97], v140 offset:7168
	ds_read_b64_tr_b16 v[100:101], v140 offset:7680
	ds_read_b64_tr_b16 v[98:99], v140 offset:6656
	s_waitcnt lgkmcnt(2)
	v_mfma_f32_32x32x16_bf16 v[18:33], v[42:45], v[94:97], v[18:33]
	ds_read_b64_tr_b16 v[94:95], v140 offset:8192
	ds_read_b64_tr_b16 v[96:97], v140 offset:9216
	ds_read_b64_tr_b16 v[104:105], v140 offset:9728
	ds_read_b64_tr_b16 v[102:103], v140 offset:8704
	v_mfma_f32_32x32x16_bf16 v[2:17], v[86:89], v[106:109], v[2:17]
	s_waitcnt lgkmcnt(2)
	v_mfma_f32_32x32x16_bf16 v[18:33], v[90:93], v[94:97], v[18:33]
	ds_read_b64_tr_b16 v[86:87], v140 offset:10240
	ds_read_b64_tr_b16 v[88:89], v140 offset:11264
	ds_read_b64_tr_b16 v[96:97], v140 offset:11776
	ds_read_b64_tr_b16 v[94:95], v140 offset:10752
	v_mfma_f32_32x32x16_bf16 v[2:17], v[54:57], v[110:113], v[2:17]
	s_waitcnt lgkmcnt(2)
	v_mfma_f32_32x32x16_bf16 v[18:33], v[78:81], v[86:89], v[18:33]
	ds_read_b64_tr_b16 v[86:87], v140 offset:12288
	ds_read_b64_tr_b16 v[88:89], v140 offset:13312
	ds_read_b64_tr_b16 v[108:109], v140 offset:13824
	ds_read_b64_tr_b16 v[106:107], v140 offset:12800
	v_mfma_f32_32x32x16_bf16 v[2:17], v[42:45], v[98:101], v[2:17]
	s_waitcnt lgkmcnt(2)
	v_mfma_f32_32x32x16_bf16 v[18:33], v[82:85], v[86:89], v[18:33]
	ds_read_b64_tr_b16 v[54:55], v140 offset:14336
	ds_read_b64_tr_b16 v[56:57], v140 offset:15360
	ds_read_b64_tr_b16 v[88:89], v140 offset:15872
	ds_read_b64_tr_b16 v[86:87], v140 offset:14848
	v_mfma_f32_32x32x16_bf16 v[2:17], v[90:93], v[102:105], v[2:17]
	s_waitcnt lgkmcnt(2)
	v_mfma_f32_32x32x16_bf16 v[18:33], v[74:77], v[54:57], v[18:33]
	ds_read_b64_tr_b16 v[54:55], v140 offset:16384
	ds_read_b64_tr_b16 v[56:57], v140 offset:17408
	ds_read_b64_tr_b16 v[112:113], v140 offset:17920
	ds_read_b64_tr_b16 v[110:111], v140 offset:16896
	v_mfma_f32_32x32x16_bf16 v[2:17], v[78:81], v[94:97], v[2:17]
	s_waitcnt lgkmcnt(2)
	v_mfma_f32_32x32x16_bf16 v[18:33], v[66:69], v[54:57], v[18:33]
	ds_read_b64_tr_b16 v[42:43], v140 offset:18432
	ds_read_b64_tr_b16 v[44:45], v140 offset:19456
	ds_read_b64_tr_b16 v[56:57], v140 offset:19968
	ds_read_b64_tr_b16 v[54:55], v140 offset:18944
	v_mfma_f32_32x32x16_bf16 v[2:17], v[82:85], v[106:109], v[2:17]
	s_waitcnt lgkmcnt(2)
	v_mfma_f32_32x32x16_bf16 v[18:33], v[70:73], v[42:45], v[18:33]
	ds_read_b64_tr_b16 v[42:43], v140 offset:20480
	ds_read_b64_tr_b16 v[44:45], v140 offset:21504
	ds_read_b64_tr_b16 v[80:81], v140 offset:22016
	ds_read_b64_tr_b16 v[78:79], v140 offset:20992
	v_mfma_f32_32x32x16_bf16 v[2:17], v[74:77], v[86:89], v[2:17]
	s_waitcnt lgkmcnt(2)
	v_mfma_f32_32x32x16_bf16 v[18:33], v[62:65], v[42:45], v[18:33]
	ds_read_b64_tr_b16 v[42:43], v140 offset:22528
	ds_read_b64_tr_b16 v[44:45], v140 offset:23552
	ds_read_b64_tr_b16 v[76:77], v140 offset:24064
	ds_read_b64_tr_b16 v[74:75], v140 offset:23040
	v_mfma_f32_32x32x16_bf16 v[2:17], v[66:69], v[110:113], v[2:17]
	s_waitcnt lgkmcnt(2)
	v_mfma_f32_32x32x16_bf16 v[18:33], v[58:61], v[42:45], v[18:33]
	v_mfma_f32_32x32x16_bf16 v[2:17], v[70:73], v[54:57], v[2:17]
	ds_read_b64_tr_b16 v[42:43], v140 offset:24576
	ds_read_b64_tr_b16 v[44:45], v140 offset:25600
	ds_read_b64_tr_b16 v[56:57], v140 offset:26112
	ds_read_b64_tr_b16 v[54:55], v140 offset:25088
	s_waitcnt lgkmcnt(2)
	v_mfma_f32_32x32x16_bf16 v[18:33], v[50:53], v[42:45], v[18:33]
	ds_read_b64_tr_b16 v[42:43], v140 offset:26624
	ds_read_b64_tr_b16 v[44:45], v140 offset:27648
	ds_read_b64_tr_b16 v[68:69], v140 offset:28160
	ds_read_b64_tr_b16 v[66:67], v140 offset:27136
	v_mfma_f32_32x32x16_bf16 v[2:17], v[62:65], v[78:81], v[2:17]
	s_waitcnt lgkmcnt(2)
	v_mfma_f32_32x32x16_bf16 v[18:33], v[46:49], v[42:45], v[18:33]
	ds_read_b64_tr_b16 v[42:43], v140 offset:28672
	ds_read_b64_tr_b16 v[44:45], v140 offset:29696
	ds_read_b64_tr_b16 v[150:151], v140 offset:30208
	ds_read_b64_tr_b16 v[148:149], v140 offset:29184
	v_mfma_f32_32x32x16_bf16 v[2:17], v[58:61], v[74:77], v[2:17]
	s_waitcnt lgkmcnt(2)
	v_mfma_f32_32x32x16_bf16 v[18:33], v[38:41], v[42:45], v[18:33]
	v_add_co_u32_e64 v42, s[4:5], s4, v132
	s_nop 1
	v_addc_co_u32_e64 v43, s[4:5], 0, v133, s[4:5]
	s_mov_b32 s4, 0x21000
	s_nop 0
	v_add_co_u32_e64 v44, s[4:5], s4, v132
	v_mfma_f32_32x32x16_bf16 v[2:17], v[50:53], v[54:57], v[2:17]
	s_nop 0
	v_addc_co_u32_e64 v45, s[4:5], 0, v133, s[4:5]
	s_mov_b32 s4, 0x22000
	s_nop 0
	v_add_co_u32_e64 v50, s[4:5], s4, v132
	global_load_dwordx4 v[122:125], v[42:43], off offset:1024
	global_load_dwordx4 v[114:117], v[42:43], off offset:2048
	global_load_dwordx4 v[126:129], v[44:45], off offset:-4096
	global_load_dwordx4 v[110:113], v[44:45], off
	global_load_dwordx4 v[106:109], v[44:45], off offset:1024
	global_load_dwordx4 v[102:105], v[44:45], off offset:2048
	v_addc_co_u32_e64 v51, s[4:5], 0, v133, s[4:5]
	s_mov_b32 s4, 0x23000
	s_nop 0
	v_add_co_u32_e64 v52, s[4:5], s4, v132
	v_mfma_f32_32x32x16_bf16 v[2:17], v[46:49], v[66:69], v[2:17]
	s_nop 0
	v_addc_co_u32_e64 v53, s[4:5], 0, v133, s[4:5]
	global_load_dwordx4 v[98:101], v[44:45], off offset:3072
	global_load_dwordx4 v[94:97], v[52:53], off offset:-4096
	global_load_dwordx4 v[118:121], v[42:43], off offset:3072
	global_load_dwordx4 v[90:93], v[50:51], off offset:1024
	global_load_dwordx4 v[86:89], v[50:51], off offset:2048
	global_load_dwordx4 v[82:85], v[50:51], off offset:3072
	global_load_dwordx4 v[70:73], v[52:53], off
	global_load_dwordx4 v[66:69], v[52:53], off offset:1024
	global_load_dwordx4 v[74:77], v[52:53], off offset:2048
	global_load_dwordx4 v[78:81], v[52:53], off offset:3072
	s_waitcnt lgkmcnt(0)
	v_mfma_f32_32x32x16_bf16 v[2:17], v[38:41], v[148:151], v[2:17]
	ds_read_b64_tr_b16 v[38:39], v140 offset:30720
	ds_read_b64_tr_b16 v[40:41], v140 offset:31744
	ds_read_b64_tr_b16 v[44:45], v140 offset:32256
	ds_read_b64_tr_b16 v[42:43], v140 offset:31232
	s_waitcnt lgkmcnt(0)
	s_barrier
	v_mfma_f32_32x32x16_bf16 v[18:33], v[34:37], v[38:41], v[18:33]
	v_lshl_add_u32 v38, v137, 2, 0
	v_mfma_f32_32x32x16_bf16 v[2:17], v[34:37], v[42:45], v[2:17]
	s_nop 9
	v_max3_f32 v39, |v18|, 0, |v19|
	v_max3_f32 v39, v39, |v20|, |v21|
	v_max3_f32 v39, v39, |v22|, |v23|
	v_max3_f32 v39, v39, |v24|, |v25|
	v_max3_f32 v39, v39, |v26|, |v27|
	v_max3_f32 v39, v39, |v28|, |v29|
	v_max3_f32 v34, v39, |v30|, |v31|
	v_max3_f32 v36, |v2|, 0, |v3|
	v_max3_f32 v36, v36, |v4|, |v5|
	v_max3_f32 v36, v36, |v6|, |v7|
	v_max3_f32 v36, v36, |v8|, |v9|
	v_max3_f32 v36, v36, |v10|, |v11|
	v_max3_f32 v36, v36, |v12|, |v13|
	v_max3_f32 v36, v36, |v14|, |v15|
	v_max3_f32 v34, v34, |v32|, |v33|
	v_max3_f32 v36, v36, |v16|, |v17|
	v_mov_b32_e32 v35, v34
	v_mov_b32_e32 v37, v36
	s_nop 0
	v_permlane32_swap_b32_e32 v34, v35
	v_permlane32_swap_b32_e32 v36, v37
	s_and_saveexec_b64 s[4:5], vcc
	s_cbranch_execz .LBB1_6
	v_max_f32_e32 v34, v34, v34
	v_max_f32_e32 v35, v35, v35
	v_max_f32_e32 v34, v34, v35
	v_and_b32_e32 v35, 0x1c0, v0
	v_max_f32_e32 v36, v36, v36
	v_max_f32_e32 v37, v37, v37
	v_lshl_add_u32 v35, v35, 2, v38
	v_max_f32_e32 v36, v36, v37
	v_add_u32_e32 v35, 0x8800, v35
	ds_write2_b32 v35, v34, v36 offset1:32

	.amdhsa_kernel _Z10qkv_kernelPKfS0_S0_PKdPKtS0_PhPfS6_
		.amdhsa_group_segment_fixed_size 0
		.amdhsa_private_segment_fixed_size 0
		.amdhsa_kernarg_size 72
		.amdhsa_user_sgpr_count 2
		.amdhsa_user_sgpr_dispatch_ptr 0
		.amdhsa_user_sgpr_queue_ptr 0
		.amdhsa_user_sgpr_kernarg_segment_ptr 1
		.amdhsa_user_sgpr_dispatch_id 0
		.amdhsa_user_sgpr_kernarg_preload_length 0
		.amdhsa_user_sgpr_kernarg_preload_offset 0
		.amdhsa_user_sgpr_private_segment_size 0
		.amdhsa_uses_dynamic_stack 0
		.amdhsa_enable_private_segment 0
		.amdhsa_system_sgpr_workgroup_id_x 1
		.amdhsa_system_sgpr_workgroup_id_y 0
		.amdhsa_system_sgpr_workgroup_id_z 0
		.amdhsa_system_sgpr_workgroup_info 0
		.amdhsa_system_vgpr_workitem_id 0
		.amdhsa_next_free_vgpr 192
		.amdhsa_next_free_sgpr 30
		.amdhsa_accum_offset 192
		.amdhsa_reserve_vcc 1
		.amdhsa_float_round_mode_32 0
		.amdhsa_float_round_mode_16_64 0
		.amdhsa_float_denorm_mode_32 3
		.amdhsa_float_denorm_mode_16_64 3
		.amdhsa_dx10_clamp 1
		.amdhsa_ieee_mode 1
		.amdhsa_fp16_overflow 0
		.amdhsa_tg_split 0
		.amdhsa_exception_fp_ieee_invalid_op 0
		.amdhsa_exception_fp_denorm_src 0
		.amdhsa_exception_fp_ieee_div_zero 0
		.amdhsa_exception_fp_ieee_overflow 0
		.amdhsa_exception_fp_ieee_underflow 0
		.amdhsa_exception_fp_ieee_inexact 0
		.amdhsa_exception_int_div_zero 0
	.end_amdhsa_kernel

amdhsa.kernels:
  - .agpr_count:     0
    .args:
      - .actual_access:  read_only
        .address_space:  global
        .offset:         0
        .size:           8
        .value_kind:     global_buffer
      - .actual_access:  read_only
        .address_space:  global
        .offset:         8
        .size:           8
        .value_kind:     global_buffer
      - .actual_access:  read_only
        .address_space:  global
        .offset:         16
        .size:           8
        .value_kind:     global_buffer
      - .actual_access:  write_only
        .address_space:  global
        .offset:         24
        .size:           8
        .value_kind:     global_buffer
      - .actual_access:  write_only
        .address_space:  global
        .offset:         32
        .size:           8
        .value_kind:     global_buffer
      - .actual_access:  write_only
        .address_space:  global
        .offset:         40
        .size:           8
        .value_kind:     global_buffer
    .group_segment_fixed_size: 512
    .kernarg_segment_align: 8
    .kernarg_segment_size: 48
    .language:       OpenCL C
    .language_version:
      - 2
      - 0
    .max_flat_workgroup_size: 1024
    .name:           _Z11prep_kernelPKfS0_S0_PdPtS2_
    .private_segment_fixed_size: 0
    .sgpr_count:     22
    .sgpr_spill_count: 0
    .symbol:         _Z11prep_kernelPKfS0_S0_PdPtS2_.kd
    .uniform_work_group_size: 1
    .uses_dynamic_stack: false
    .vgpr_count:     32
    .vgpr_spill_count: 0
    .wavefront_size: 64
  - .agpr_count:     0
    .args:
      - .actual_access:  read_only
        .address_space:  global
        .offset:         0
        .size:           8
        .value_kind:     global_buffer
      - .actual_access:  read_only
        .address_space:  global
        .offset:         8
        .size:           8
        .value_kind:     global_buffer
      - .actual_access:  read_only
        .address_space:  global
        .offset:         16
        .size:           8
        .value_kind:     global_buffer
      - .actual_access:  read_only
        .address_space:  global
        .offset:         24
        .size:           8
        .value_kind:     global_buffer
      - .actual_access:  read_only
        .address_space:  global
        .offset:         32
        .size:           8
        .value_kind:     global_buffer
      - .actual_access:  read_only
        .address_space:  global
        .offset:         40
        .size:           8
        .value_kind:     global_buffer
      - .actual_access:  write_only
        .address_space:  global
        .offset:         48
        .size:           8
        .value_kind:     global_buffer
      - .actual_access:  write_only
        .address_space:  global
        .offset:         56
        .size:           8
        .value_kind:     global_buffer
      - .actual_access:  write_only
        .address_space:  global
        .offset:         64
        .size:           8
        .value_kind:     global_buffer
    .group_segment_fixed_size: 0
    .kernarg_segment_align: 8
    .kernarg_segment_size: 72
    .language:       OpenCL C
    .language_version:
      - 2
      - 0
    .max_flat_workgroup_size: 512
    .name:           _Z10qkv_kernelPKfS0_S0_PKdPKtS0_PhPfS6_
    .private_segment_fixed_size: 0
    .sgpr_count:     36
    .sgpr_spill_count: 0
    .symbol:         _Z10qkv_kernelPKfS0_S0_PKdPKtS0_PhPfS6_.kd
    .uniform_work_group_size: 1
    .uses_dynamic_stack: false
    .vgpr_count:     192
    .vgpr_spill_count: 0
    .wavefront_size: 64
  - .agpr_count:     0
    .args:
      - .actual_access:  read_only
        .address_space:  global
        .offset:         0
        .size:           8
        .value_kind:     global_buffer
      - .address_space:  global
        .offset:         8
        .size:           8
        .value_kind:     global_buffer
      - .address_space:  global
        .offset:         16
        .size:           8
        .value_kind:     global_buffer
      - .actual_access:  read_only
        .address_space:  global
        .offset:         24
        .size:           8
        .value_kind:     global_buffer
      - .actual_access:  read_only
        .address_space:  global
        .offset:         32
        .size:           8
        .value_kind:     global_buffer
      - .actual_access:  write_only
        .address_space:  global
        .offset:         40
        .size:           8
        .value_kind:     global_buffer
      - .actual_access:  write_only
        .address_space:  global
        .offset:         48
        .size:           8
        .value_kind:     global_buffer
      - .actual_access:  write_only
        .address_space:  global
        .offset:         56
        .size:           8
        .value_kind:     global_buffer
    .group_segment_fixed_size: 0
    .kernarg_segment_align: 8
    .kernarg_segment_size: 64
    .language:       OpenCL C
    .language_version:
      - 2
      - 0
    .max_flat_workgroup_size: 512
    .name:           _Z11attn_kernelPKhS0_S0_PKfS2_PhPfS4_
    .private_segment_fixed_size: 0
    .sgpr_count:     72
    .sgpr_spill_count: 0
    .symbol:         _Z11attn_kernelPKhS0_S0_PKfS2_PhPfS4_.kd
    .uniform_work_group_size: 1
    .uses_dynamic_stack: false
    .vgpr_count:     256
    .vgpr_spill_count: 0
    .wavefront_size: 64
  - .agpr_count:     0
    .args:
      - .actual_access:  read_only
        .address_space:  global
        .offset:         0
        .size:           8
        .value_kind:     global_buffer
      - .actual_access:  read_only
        .address_space:  global
        .offset:         8
        .size:           8
        .value_kind:     global_buffer
      - .actual_access:  read_only
        .address_space:  global
        .offset:         16
        .size:           8
        .value_kind:     global_buffer
      - .actual_access:  read_only
        .address_space:  global
        .offset:         24
        .size:           8
        .value_kind:     global_buffer
      - .actual_access:  read_only
        .address_space:  global
        .offset:         32
        .size:           8
        .value_kind:     global_buffer
      - .actual_access:  read_only
        .address_space:  global
        .offset:         40
        .size:           8
        .value_kind:     global_buffer
      - .actual_access:  write_only
        .address_space:  global
        .offset:         48
        .size:           8
        .value_kind:     global_buffer
    .group_segment_fixed_size: 16640
    .kernarg_segment_align: 8
    .kernarg_segment_size: 56
    .language:       OpenCL C
    .language_version:
      - 2
      - 0
    .max_flat_workgroup_size: 512
    .name:           _Z14outproj_kernelPKhPKfS2_PKtS2_S2_Pf
    .private_segment_fixed_size: 0
    .sgpr_count:     24
    .sgpr_spill_count: 0
    .symbol:         _Z14outproj_kernelPKhPKfS2_PKtS2_S2_Pf.kd
    .uniform_work_group_size: 1
    .uses_dynamic_stack: false
    .vgpr_count:     109
    .vgpr_spill_count: 0
    .wavefront_size: 64
